# speedup vs baseline: 1.0073x; 1.0073x over previous
_Z6k_pre1PKiPiPKfS3_S3_S3_S3_S3_S3_S3_S3_PDF16_S4_S4_PfS5_:
	s_cmpk_gt_u32 s2, 0xff
	s_mov_b64 s[4:5], -1
	s_cbranch_scc0 .LBB0_14
	s_lshl_b32 s3, s2, 10
	s_add_i32 s3, s3, 0xfffc0000
	v_or_b32_e32 v2, s3, v0
	s_mov_b32 s4, 0x24600
	v_cmp_gt_i32_e32 vcc, s4, v2
	s_and_saveexec_b64 s[4:5], vcc
	s_cbranch_execz .LBB0_13
	s_load_dwordx2 s[6:7], s[0:1], 0x10
	s_movk_i32 s8, 0x3fff
	v_cmp_lt_i32_e32 vcc, s8, v2
	s_and_saveexec_b64 s[8:9], vcc
	s_xor_b64 s[8:9], exec, s[8:9]
	s_cbranch_execz .LBB0_11
	s_cmp_gt_u32 s3, 0x23fff
	s_mov_b64 s[10:11], -1
	s_cbranch_scc0 .LBB0_9
	s_mov_b64 s[10:11], exec
	s_load_dwordx4 s[12:15], s[0:1], 0x18
	s_load_dwordx4 s[16:19], s[0:1], 0x70
	v_add_u32_e32 v4, 0xfffdc000, v2
	v_cmp_gt_u32_e32 vcc, 0x400, v4
	s_and_b64 exec, exec, vcc
	s_cbranch_execz .Lpre1_dot_done
	v_lshrrev_b32_e32 v5, 1, v4
	v_and_b32_e32 v1, 1, v4
	v_lshrrev_b32_e32 v6, 3, v5
	v_and_b32_e32 v7, 3, v5
	v_lshlrev_b32_e32 v6, 8, v6
	v_lshl_add_u32 v6, v7, 6, v6
	v_lshl_add_u32 v6, v1, 5, v6
	v_lshlrev_b32_e32 v6, 2, v6
	v_lshlrev_b32_e32 v7, 6, v7
	v_lshl_add_u32 v7, v1, 5, v7
	v_lshlrev_b32_e32 v7, 2, v7
	v_and_b32_e32 v3, 4, v5
	v_cmp_eq_u32_e32 vcc, 0, v3
	s_waitcnt lgkmcnt(0)
	v_mov_b32_e32 v8, s12
	v_mov_b32_e32 v9, s14
	v_cndmask_b32_e32 v8, v9, v8, vcc
	v_mov_b32_e32 v9, s13
	v_mov_b32_e32 v10, s15
	v_cndmask_b32_e32 v9, v10, v9, vcc
	v_add_co_u32_e32 v8, vcc, v8, v7
	s_nop 1
	v_addc_co_u32_e32 v9, vcc, 0, v9, vcc
	global_load_dwordx4 v[12:15], v6, s[6:7] offset:0
	global_load_dwordx4 v[16:19], v6, s[6:7] offset:16
	global_load_dwordx4 v[20:23], v6, s[6:7] offset:32
	global_load_dwordx4 v[24:27], v6, s[6:7] offset:48
	global_load_dwordx4 v[28:31], v6, s[6:7] offset:64
	global_load_dwordx4 v[32:35], v6, s[6:7] offset:80
	global_load_dwordx4 v[36:39], v6, s[6:7] offset:96
	global_load_dwordx4 v[40:43], v6, s[6:7] offset:112
	global_load_dwordx4 v[44:47], v[8:9], off offset:0
	global_load_dwordx4 v[48:51], v[8:9], off offset:16
	global_load_dwordx4 v[52:55], v[8:9], off offset:32
	global_load_dwordx4 v[56:59], v[8:9], off offset:48
	v_lshlrev_b32_e32 v3, 2, v4
	v_mov_b32_e32 v10, 0
	global_store_dword v3, v10, s[18:19]
	s_waitcnt vmcnt(1)
	v_fmac_f32_e32 v10, v12, v44
	v_fmac_f32_e32 v10, v13, v45
	v_fmac_f32_e32 v10, v14, v46
	v_fmac_f32_e32 v10, v15, v47
	v_fmac_f32_e32 v10, v16, v48
	v_fmac_f32_e32 v10, v17, v49
	v_fmac_f32_e32 v10, v18, v50
	v_fmac_f32_e32 v10, v19, v51
	v_fmac_f32_e32 v10, v20, v52
	v_fmac_f32_e32 v10, v21, v53
	v_fmac_f32_e32 v10, v22, v54
	v_fmac_f32_e32 v10, v23, v55
	v_fmac_f32_e32 v10, v24, v56
	v_fmac_f32_e32 v10, v25, v57
	v_fmac_f32_e32 v10, v26, v58
	v_fmac_f32_e32 v10, v27, v59
	global_load_dwordx4 v[44:47], v[8:9], off offset:64
	global_load_dwordx4 v[48:51], v[8:9], off offset:80
	global_load_dwordx4 v[52:55], v[8:9], off offset:96
	global_load_dwordx4 v[56:59], v[8:9], off offset:112
	s_waitcnt vmcnt(0)
	v_fmac_f32_e32 v10, v28, v44
	v_fmac_f32_e32 v10, v29, v45
	v_fmac_f32_e32 v10, v30, v46
	v_fmac_f32_e32 v10, v31, v47
	v_fmac_f32_e32 v10, v32, v48
	v_fmac_f32_e32 v10, v33, v49
	v_fmac_f32_e32 v10, v34, v50
	v_fmac_f32_e32 v10, v35, v51
	v_fmac_f32_e32 v10, v36, v52
	v_fmac_f32_e32 v10, v37, v53
	v_fmac_f32_e32 v10, v38, v54
	v_fmac_f32_e32 v10, v39, v55
	v_fmac_f32_e32 v10, v40, v56
	v_fmac_f32_e32 v10, v41, v57
	v_fmac_f32_e32 v10, v42, v58
	v_fmac_f32_e32 v10, v43, v59
	s_nop 1
	v_add_f32_dpp v11, v10, v10 quad_perm:[1,0,3,2] row_mask:0xf bank_mask:0xf
	v_cmp_eq_u32_e32 vcc, 0, v1
	s_and_b64 exec, exec, vcc
	v_lshlrev_b32_e32 v3, 2, v5
	global_store_dword v3, v11, s[16:17]
.Lpre1_dot_done:
.LBB0_8:
	s_or_b64 exec, exec, s[10:11]
	s_mov_b64 s[10:11], 0

	.amdhsa_kernel _Z6k_pre1PKiPiPKfS3_S3_S3_S3_S3_S3_S3_S3_PDF16_S4_S4_PfS5_
		.amdhsa_group_segment_fixed_size 1564
		.amdhsa_private_segment_fixed_size 0
		.amdhsa_kernarg_size 128
		.amdhsa_user_sgpr_count 2
		.amdhsa_user_sgpr_dispatch_ptr 0
		.amdhsa_user_sgpr_queue_ptr 0
		.amdhsa_user_sgpr_kernarg_segment_ptr 1
		.amdhsa_user_sgpr_dispatch_id 0
		.amdhsa_user_sgpr_kernarg_preload_length 0
		.amdhsa_user_sgpr_kernarg_preload_offset 0
		.amdhsa_user_sgpr_private_segment_size 0
		.amdhsa_uses_dynamic_stack 0
		.amdhsa_enable_private_segment 0
		.amdhsa_system_sgpr_workgroup_id_x 1
		.amdhsa_system_sgpr_workgroup_id_y 0
		.amdhsa_system_sgpr_workgroup_id_z 0
		.amdhsa_system_sgpr_workgroup_info 0
		.amdhsa_system_vgpr_workitem_id 0
		.amdhsa_next_free_vgpr 64
		.amdhsa_next_free_sgpr 20
		.amdhsa_accum_offset 64
		.amdhsa_reserve_vcc 1
		.amdhsa_float_round_mode_32 0
		.amdhsa_float_round_mode_16_64 0
		.amdhsa_float_denorm_mode_32 3
		.amdhsa_float_denorm_mode_16_64 3
		.amdhsa_dx10_clamp 1
		.amdhsa_ieee_mode 1
		.amdhsa_fp16_overflow 0
		.amdhsa_tg_split 0
		.amdhsa_exception_fp_ieee_invalid_op 0
		.amdhsa_exception_fp_denorm_src 0
		.amdhsa_exception_fp_ieee_div_zero 0
		.amdhsa_exception_fp_ieee_overflow 0
		.amdhsa_exception_fp_ieee_underflow 0
		.amdhsa_exception_fp_ieee_inexact 0
		.amdhsa_exception_int_div_zero 0
	.end_amdhsa_kernel

_Z9k_scatterPKiS0_S0_S0_PiS1_:
	s_load_dwordx4 s[4:7], s[0:1], 0x0
	s_load_dwordx2 s[12:13], s[0:1], 0x18
	s_load_dwordx2 s[14:15], s[0:1], 0x10
	s_mul_i32 s3, s2, 0x186a
	v_add_u32_e32 v2, s3, v0
	v_ashrrev_i32_e32 v3, 31, v2
	v_lshlrev_b64 v[4:5], 2, v[2:3]
	s_waitcnt lgkmcnt(0)
	v_mov_b32_e32 v31, 0
	v_mov_b32_e32 v33, 0
	v_lshlrev_b32_e32 v32, 2, v0
	v_cmp_gt_u32_e32 vcc, 0x187, v0
	s_and_saveexec_b64 s[10:11], vcc
	global_load_dword v31, v32, s[12:13]
	v_lshl_add_u32 v34, v0, 8, s2
	v_lshlrev_b32_e32 v34, 2, v34
	global_load_dword v33, v34, s[14:15]
	s_or_b64 exec, exec, s[10:11]
	v_lshl_add_u64 v[6:7], s[6:7], 0, v[4:5]
	v_lshl_add_u64 v[4:5], s[4:5], 0, v[4:5]
	global_load_dword v30, v[4:5], off
	v_add_u32_e32 v4, 0x400, v2
	v_ashrrev_i32_e32 v5, 31, v4
	v_lshlrev_b64 v[4:5], 2, v[4:5]
	global_load_dword v29, v[6:7], off
	v_lshl_add_u64 v[6:7], s[6:7], 0, v[4:5]
	v_lshl_add_u64 v[4:5], s[4:5], 0, v[4:5]
	global_load_dword v28, v[4:5], off
	v_add_u32_e32 v4, 0x800, v2
	v_ashrrev_i32_e32 v5, 31, v4
	v_lshlrev_b64 v[4:5], 2, v[4:5]
	global_load_dword v27, v[6:7], off
	v_lshl_add_u64 v[6:7], s[6:7], 0, v[4:5]
	v_lshl_add_u64 v[4:5], s[4:5], 0, v[4:5]
	global_load_dword v26, v[4:5], off
	v_add_u32_e32 v4, 0xc00, v2
	v_ashrrev_i32_e32 v5, 31, v4
	v_lshlrev_b64 v[4:5], 2, v[4:5]
	global_load_dword v25, v[6:7], off
	v_lshl_add_u64 v[6:7], s[6:7], 0, v[4:5]
	v_lshl_add_u64 v[4:5], s[4:5], 0, v[4:5]
	global_load_dword v24, v[4:5], off
	v_add_u32_e32 v4, 0x1000, v2
	v_ashrrev_i32_e32 v5, 31, v4
	v_add_u32_e32 v2, 0x1400, v2
	v_lshlrev_b64 v[4:5], 2, v[4:5]
	v_ashrrev_i32_e32 v3, 31, v2
	global_load_dword v23, v[6:7], off
	v_lshl_add_u64 v[6:7], s[6:7], 0, v[4:5]
	v_lshl_add_u64 v[4:5], s[4:5], 0, v[4:5]
	v_lshlrev_b64 v[2:3], 2, v[2:3]
	global_load_dword v22, v[4:5], off
	v_lshl_add_u64 v[4:5], s[6:7], 0, v[2:3]
	v_lshl_add_u64 v[2:3], s[4:5], 0, v[2:3]
	global_load_dword v21, v[6:7], off
	global_load_dword v18, v[4:5], off
	global_load_dword v19, v[2:3], off
	s_movk_i32 s8, 0x186a
	v_or_b32_e32 v2, 0x1800, v0
	v_cmp_gt_u32_e32 vcc, s8, v2
	v_add_u32_e32 v2, s3, v2
	v_mov_b32_e32 v1, -1
	v_ashrrev_i32_e32 v3, 31, v2
	s_and_saveexec_b64 s[8:9], vcc
	s_cbranch_execz .LBB1_2
	v_lshl_add_u64 v[4:5], v[2:3], 2, s[6:7]
	global_load_dword v1, v[4:5], off
.LBB1_2:
	s_or_b64 exec, exec, s[8:9]
	v_mov_b32_e32 v20, 0
	s_and_saveexec_b64 s[6:7], vcc
	s_cbranch_execz .LBB1_4
	v_lshl_add_u64 v[2:3], v[2:3], 2, s[4:5]
	global_load_dword v20, v[2:3], off
.LBB1_4:
	s_or_b64 exec, exec, s[6:7]
	s_movk_i32 s3, 0x187
	v_cmp_gt_u32_e32 vcc, s3, v0
	v_lshlrev_b32_e32 v32, 2, v0
	v_mbcnt_lo_u32_b32 v2, -1, 0
	v_mbcnt_hi_u32_b32 v2, -1, v2
	v_and_b32_e32 v3, 64, v2
	v_add_u32_e32 v4, -1, v2
	v_cmp_lt_i32_e64 s[4:5], v4, v3
	v_and_b32_e32 v5, 63, v0
	v_add_u32_e32 v6, -2, v2
	v_cndmask_b32_e64 v4, v4, v2, s[4:5]
	v_lshlrev_b32_e32 v4, 2, v4
	s_waitcnt vmcnt(12)
	ds_bpermute_b32 v4, v4, v31
	v_cmp_ne_u32_e64 s[4:5], 0, v5
	s_load_dwordx2 s[6:7], s[0:1], 0x20
	v_lshrrev_b32_e32 v34, 6, v0
	s_waitcnt lgkmcnt(0)
	v_cndmask_b32_e64 v4, 0, v4, s[4:5]
	v_cmp_lt_i32_e64 s[4:5], v6, v3
	v_add_u32_e32 v4, v4, v31
	s_nop 0
	v_cndmask_b32_e64 v6, v6, v2, s[4:5]
	v_lshlrev_b32_e32 v6, 2, v6
	ds_bpermute_b32 v6, v6, v4
	v_cmp_lt_u32_e64 s[4:5], 1, v5
	s_waitcnt lgkmcnt(0)
	s_nop 0
	v_cndmask_b32_e64 v6, 0, v6, s[4:5]
	v_add_u32_e32 v4, v6, v4
	v_add_u32_e32 v6, -4, v2
	v_cmp_lt_i32_e64 s[4:5], v6, v3
	s_nop 1
	v_cndmask_b32_e64 v6, v6, v2, s[4:5]
	v_lshlrev_b32_e32 v6, 2, v6
	ds_bpermute_b32 v6, v6, v4
	v_cmp_lt_u32_e64 s[4:5], 3, v5
	s_waitcnt lgkmcnt(0)
	s_nop 0
	v_cndmask_b32_e64 v6, 0, v6, s[4:5]
	v_add_u32_e32 v4, v6, v4
	v_add_u32_e32 v6, -8, v2
	v_cmp_lt_i32_e64 s[4:5], v6, v3
	s_nop 1
	v_cndmask_b32_e64 v6, v6, v2, s[4:5]
	v_lshlrev_b32_e32 v6, 2, v6
	ds_bpermute_b32 v6, v6, v4
	v_cmp_lt_u32_e64 s[4:5], 7, v5
	s_waitcnt lgkmcnt(0)
	s_nop 0
	v_cndmask_b32_e64 v6, 0, v6, s[4:5]
	v_add_u32_e32 v4, v6, v4
	v_add_u32_e32 v6, -16, v2
	v_cmp_lt_i32_e64 s[4:5], v6, v3
	s_nop 1
	v_cndmask_b32_e64 v6, v6, v2, s[4:5]
	v_lshlrev_b32_e32 v6, 2, v6
	ds_bpermute_b32 v6, v6, v4
	v_cmp_lt_u32_e64 s[4:5], 15, v5
	s_waitcnt lgkmcnt(0)
	s_nop 0
	v_cndmask_b32_e64 v6, 0, v6, s[4:5]
	v_add_u32_e32 v4, v6, v4
	v_subrev_u32_e32 v6, 32, v2
	v_cmp_lt_i32_e64 s[4:5], v6, v3
	s_nop 1
	v_cndmask_b32_e64 v2, v6, v2, s[4:5]
	v_lshlrev_b32_e32 v2, 2, v2
	ds_bpermute_b32 v2, v2, v4
	v_cmp_lt_u32_e64 s[4:5], 31, v5
	s_waitcnt lgkmcnt(0)
	s_nop 0
	v_cndmask_b32_e64 v2, 0, v2, s[4:5]
	v_add_u32_e32 v35, v2, v4
	v_cmp_eq_u32_e64 s[4:5], 63, v5
	s_and_saveexec_b64 s[8:9], s[4:5]
	v_lshlrev_b32_e32 v2, 2, v34
	ds_write_b32 v2, v35 offset:1568
	s_or_b64 exec, exec, s[8:9]
	v_mov_b32_e32 v2, 0
	s_waitcnt lgkmcnt(0)
	s_barrier
	ds_read_b128 v[14:17], v2 offset:1568
	ds_read_b128 v[10:13], v2 offset:1584
	ds_read_b128 v[6:9], v2 offset:1600
	ds_read_b128 v[2:5], v2 offset:1616
	s_waitcnt lgkmcnt(0)
	s_barrier
	s_and_saveexec_b64 s[4:5], vcc
	s_cbranch_execz .LBB1_13
	v_cmp_lt_u32_e32 vcc, 63, v0
	s_movk_i32 s3, 0x7f
	v_sub_u32_e32 v31, v35, v31
	v_cndmask_b32_e32 v36, 0, v14, vcc
	v_cmp_lt_u32_e32 vcc, s3, v0
	s_movk_i32 s3, 0xbf
	v_add_u32_e32 v31, v36, v31
	v_cndmask_b32_e32 v37, 0, v15, vcc
	v_cmp_lt_u32_e32 vcc, s3, v0
	s_movk_i32 s3, 0xff
	s_cmp_lg_u32 s2, 0
	v_cndmask_b32_e32 v38, 0, v16, vcc
	v_cmp_lt_u32_e32 vcc, s3, v0
	s_movk_i32 s3, 0x13f
	v_add3_u32 v31, v31, v37, v38
	v_cndmask_b32_e32 v39, 0, v17, vcc
	v_cmp_lt_u32_e32 vcc, s3, v0
	s_movk_i32 s3, 0x17f
	s_nop 0
	v_cndmask_b32_e32 v40, 0, v10, vcc
	v_cmp_lt_u32_e32 vcc, s3, v0
	s_movk_i32 s3, 0x1bf
	v_add3_u32 v31, v31, v39, v40
	v_cndmask_b32_e32 v41, 0, v11, vcc
	v_cmp_lt_u32_e32 vcc, s3, v0
	s_movk_i32 s3, 0x1ff
	s_nop 0
	v_cndmask_b32_e32 v42, 0, v12, vcc
	v_cmp_lt_u32_e32 vcc, s3, v0
	s_movk_i32 s3, 0x23f
	v_add3_u32 v31, v31, v41, v42
	v_cndmask_b32_e32 v43, 0, v13, vcc
	v_cmp_lt_u32_e32 vcc, s3, v0
	s_movk_i32 s3, 0x27f
	s_nop 0
	v_cndmask_b32_e32 v44, 0, v6, vcc
	v_cmp_lt_u32_e32 vcc, s3, v0
	s_movk_i32 s3, 0x2bf
	v_add3_u32 v31, v31, v43, v44
	v_cndmask_b32_e32 v45, 0, v7, vcc
	v_cmp_lt_u32_e32 vcc, s3, v0
	s_movk_i32 s3, 0x2ff
	s_nop 0
	v_cndmask_b32_e32 v46, 0, v8, vcc
	v_cmp_lt_u32_e32 vcc, s3, v0
	s_movk_i32 s3, 0x33f
	v_add3_u32 v31, v31, v45, v46
	v_cndmask_b32_e32 v47, 0, v9, vcc
	v_cmp_lt_u32_e32 vcc, s3, v0
	s_movk_i32 s3, 0x37f
	s_nop 0
	v_cndmask_b32_e32 v48, 0, v2, vcc
	v_cmp_lt_u32_e32 vcc, s3, v0
	v_add3_u32 v31, v31, v47, v48
	s_nop 0
	v_cndmask_b32_e32 v49, 0, v3, vcc
	v_cmp_eq_u32_e32 vcc, 15, v34
	s_nop 1
	v_cndmask_b32_e32 v34, 0, v4, vcc
	v_add3_u32 v31, v31, v49, v34
	v_add_u32_e32 v33, v31, v33
	ds_write_b32 v32, v33
	s_cbranch_scc1 .LBB1_13
	global_store_dword v32, v31, s[6:7]

.LBB1_15:
	s_or_b64 exec, exec, s[2:3]
	s_waitcnt vmcnt(0)
	v_lshlrev_b32_e32 v20, 8, v20
	v_cmp_lt_i32_e32 vcc, -1, v29
	s_waitcnt lgkmcnt(0)
	s_barrier
	s_and_saveexec_b64 s[2:3], vcc
	s_cbranch_execnz .LBB1_23
	s_or_b64 exec, exec, s[2:3]
	v_cmp_lt_i32_e32 vcc, -1, v27
	s_and_saveexec_b64 s[2:3], vcc
	s_cbranch_execnz .LBB1_24

	.amdhsa_kernel _Z9k_scatterPKiS0_S0_S0_PiS1_
		.amdhsa_group_segment_fixed_size 1632
		.amdhsa_private_segment_fixed_size 0
		.amdhsa_kernarg_size 48
		.amdhsa_user_sgpr_count 2
		.amdhsa_user_sgpr_dispatch_ptr 0
		.amdhsa_user_sgpr_queue_ptr 0
		.amdhsa_user_sgpr_kernarg_segment_ptr 1
		.amdhsa_user_sgpr_dispatch_id 0
		.amdhsa_user_sgpr_kernarg_preload_length 0
		.amdhsa_user_sgpr_kernarg_preload_offset 0
		.amdhsa_user_sgpr_private_segment_size 0
		.amdhsa_uses_dynamic_stack 0
		.amdhsa_enable_private_segment 0
		.amdhsa_system_sgpr_workgroup_id_x 1
		.amdhsa_system_sgpr_workgroup_id_y 0
		.amdhsa_system_sgpr_workgroup_id_z 0
		.amdhsa_system_sgpr_workgroup_info 0
		.amdhsa_system_vgpr_workitem_id 0
		.amdhsa_next_free_vgpr 50
		.amdhsa_next_free_sgpr 16
		.amdhsa_accum_offset 52
		.amdhsa_reserve_vcc 1
		.amdhsa_float_round_mode_32 0
		.amdhsa_float_round_mode_16_64 0
		.amdhsa_float_denorm_mode_32 3
		.amdhsa_float_denorm_mode_16_64 3
		.amdhsa_dx10_clamp 1
		.amdhsa_ieee_mode 1
		.amdhsa_fp16_overflow 0
		.amdhsa_tg_split 0
		.amdhsa_exception_fp_ieee_invalid_op 0
		.amdhsa_exception_fp_denorm_src 0
		.amdhsa_exception_fp_ieee_div_zero 0
		.amdhsa_exception_fp_ieee_overflow 0
		.amdhsa_exception_fp_ieee_underflow 0
		.amdhsa_exception_fp_ieee_inexact 0
		.amdhsa_exception_int_div_zero 0
	.end_amdhsa_kernel

_Z7k_layerILi0EEvPKiS1_PKfS3_PKDF16_S3_S5_S5_PDF16_P15HIP_vector_typeIfLj4EES9_S3_S3_S3_S3_S3_S3_PfSA_:
	s_setprio 1
	s_load_dwordx4 s[4:7], s[0:1], 0x20
	s_load_dwordx8 s[8:15], s[0:1], 0x38
	s_load_dwordx8 s[16:23], s[0:1], 0x0
	s_movk_i32 s3, 0x200
	v_readfirstlane_b32 s49, v0
	s_waitcnt lgkmcnt(0)
	s_mov_b64 s[24:25], s[4:5]
	v_cmp_gt_u32_e32 vcc, s3, v0
	v_lshlrev_b32_e32 v6, 2, v0
	s_and_saveexec_b64 s[4:5], vcc
	s_cbranch_execz .LBB5_3
	s_load_dwordx4 s[28:31], s[0:1], 0x58
	v_lshlrev_b32_e32 v83, 2, v0
	s_waitcnt lgkmcnt(0)
	global_load_dword v85, v83, s[28:29]
	global_load_dword v84, v83, s[30:31]
	v_add_u32_e32 v83, 0x6400, v83

.LBB5_47:
	s_and_b64 vcc, exec, s[16:17]
	s_cbranch_vccz .LBB5_66
	s_waitcnt vmcnt(7)
	v_cvt_f32_f16_e32 v2, v64
	s_waitcnt vmcnt(6)
	v_cvt_f32_f16_e32 v3, v63
	v_cmp_gt_i32_e32 vcc, s54, v35
	s_waitcnt vmcnt(5)
	s_and_saveexec_b64 s[16:17], s[2:3]
	ds_write_b32 v47, v60
	ds_write_b32 v48, v61 offset:64
	s_or_b64 exec, exec, s[16:17]
	s_add_i32 s60, s54, 7
	s_ashr_i32 s60, s60, 3
	ds_read2_b32 v[70:71], v49 offset1:4
	ds_read2_b32 v[74:75], v49 offset0:8 offset1:12
	ds_read2_b32 v[78:79], v49 offset0:16 offset1:20
	ds_read2_b32 v[82:83], v49 offset0:24 offset1:28
	s_cmp_lt_i32 s60, 1
	s_cbranch_scc1 .Lrb_done
	s_waitcnt lgkmcnt(0)
	v_lshl_or_b32 v6, v70, 7, v44
	v_lshl_or_b32 v7, v71, 7, v44
	buffer_load_dwordx2 v[70:71], v6, s[24:27], 0 offen
	buffer_load_dwordx2 v[72:73], v7, s[24:27], 0 offen
	s_cmp_lt_i32 s60, 2
	s_cbranch_scc1 .Lrb_done
	v_lshl_or_b32 v6, v74, 7, v44
	v_lshl_or_b32 v7, v75, 7, v44
	buffer_load_dwordx2 v[74:75], v6, s[24:27], 0 offen
	buffer_load_dwordx2 v[76:77], v7, s[24:27], 0 offen
	s_cmp_lt_i32 s60, 3
	s_cbranch_scc1 .Lrb_done
	v_lshl_or_b32 v10, v78, 7, v44
	v_lshl_or_b32 v11, v79, 7, v44
	buffer_load_dwordx2 v[78:79], v10, s[24:27], 0 offen
	buffer_load_dwordx2 v[80:81], v11, s[24:27], 0 offen
	s_cmp_lt_i32 s60, 4
	s_cbranch_scc1 .Lrb_done
	v_lshl_or_b32 v10, v82, 7, v44
	v_lshl_or_b32 v11, v83, 7, v44
	buffer_load_dwordx2 v[82:83], v10, s[24:27], 0 offen
	buffer_load_dwordx2 v[84:85], v11, s[24:27], 0 offen
.Lrb_done:
	v_add_f32_e32 v2, v62, v2
	v_add_f32_e32 v3, v62, v3
	v_mul_f32_e32 v4, 0x3e4ccccd, v2
	v_max_f32_e32 v2, v2, v4
	v_mul_f32_e32 v4, 0x3e4ccccd, v3
	v_cndmask_b32_e32 v2, v54, v2, vcc
	v_max_f32_e32 v3, v3, v4
	v_cmp_gt_i32_e32 vcc, s54, v36
	s_nop 1
	v_cndmask_b32_e32 v3, v54, v3, vcc
	v_max_f32_e32 v4, v2, v3
	s_nop 1
	v_max_f32_dpp v4, v4, v4 quad_perm:[1,0,3,2] row_mask:0xf bank_mask:0xf
	s_nop 0
	s_nop 1
	v_max_f32_dpp v4, v4, v4 quad_perm:[2,3,0,1] row_mask:0xf bank_mask:0xf
	s_nop 0
	s_nop 1
	v_max_f32_dpp v4, v4, v4 row_half_mirror row_mask:0xf bank_mask:0xf
	s_nop 0
	s_nop 1
	v_max_f32_dpp v4, v4, v4 row_mirror row_mask:0xf bank_mask:0xf
	s_nop 0
	v_sub_f32_e32 v2, v2, v4
	v_sub_f32_e32 v3, v3, v4
	v_mul_f32_e32 v2, 0x3fb8aa3b, v2
	v_mul_f32_e32 v3, 0x3fb8aa3b, v3
	v_exp_f32_e32 v2, v2
	v_exp_f32_e32 v3, v3
	s_nop 0
	v_add_f32_e32 v4, v2, v3
	s_nop 1
	v_add_f32_dpp v4, v4, v4 quad_perm:[1,0,3,2] row_mask:0xf bank_mask:0xf
	s_nop 0
	s_nop 1
	v_add_f32_dpp v4, v4, v4 quad_perm:[2,3,0,1] row_mask:0xf bank_mask:0xf
	s_nop 0
	s_nop 1
	v_add_f32_dpp v4, v4, v4 row_half_mirror row_mask:0xf bank_mask:0xf
	s_nop 0
	s_nop 1
	v_add_f32_dpp v4, v4, v4 row_mirror row_mask:0xf bank_mask:0xf
	s_nop 0
	v_rcp_f32_e32 v4, v4
	s_nop 0
	v_fma_mixlo_f16 v2, v2, v4, 0
	ds_write_b16 v43, v2
	v_fma_mixlo_f16 v2, v3, v4, 0
	ds_write_b16 v43, v2 offset:32
.LBB5_50:
	s_add_i32 s54, s54, 7
	s_ashr_i32 s54, s54, 3
	s_cmp_gt_i32 s54, 0
	s_cselect_b64 s[44:45], -1, 0
	s_cmp_gt_i32 s54, 1
	s_cselect_b64 s[46:47], -1, 0
	s_cmp_gt_i32 s54, 2
	s_cselect_b64 s[16:17], -1, 0
	s_cmp_gt_i32 s54, 3
	s_cselect_b64 s[22:23], -1, 0
.LBB5_58:
	s_andn2_b64 vcc, exec, s[44:45]
	v_add_u32_e32 v30, v46, v50
	s_cbranch_vccnz .LBB5_65
	s_andn2_b64 vcc, exec, s[46:47]
	s_waitcnt vmcnt(0)
	ds_write2_b64 v30, v[70:71], v[72:73] offset1:68
	s_cbranch_vccnz .LBB5_61
	ds_write2_b64 v30, v[74:75], v[76:77] offset0:136 offset1:204

.LBB5_62:
	s_andn2_b64 vcc, exec, s[22:23]
	ds_write2_b64 v30, v[78:79], v[80:81] offset1:68
	s_cbranch_vccnz .LBB5_64
	ds_write2_b64 v30, v[82:83], v[84:85] offset0:136 offset1:204

.LBB5_68:
	s_setprio 0
	s_lshl_b32 s0, s33, 2
	v_lshlrev_b32_e32 v70, 4, v1
	s_mov_b32 s1, 0
	v_mov_b32_e32 v71, 0
	s_waitcnt lgkmcnt(0)
	v_lshl_add_u64 v[6:7], s[34:35], 0, v[70:71]
	s_lshl_b64 s[2:3], s[0:1], 10
	v_lshl_add_u64 v[10:11], v[6:7], 0, s[2:3]
	global_load_dwordx4 v[2:5], v[10:11], off
	s_add_i32 s0, s0, 16
	s_lshl_b64 s[2:3], s[0:1], 10
	v_lshl_add_u64 v[12:13], v[6:7], 0, s[2:3]
	global_load_dwordx4 v[6:9], v[12:13], off
	global_load_dwordx4 v[42:45], v[10:11], off offset:1024
	global_load_dwordx4 v[46:49], v[12:13], off offset:1024
	global_load_dwordx4 v[50:53], v[10:11], off offset:2048
	global_load_dwordx4 v[54:57], v[12:13], off offset:2048
	global_load_dwordx4 v[38:41], v[10:11], off offset:3072
	v_lshrrev_b32_e32 v66, 5, v1
	v_and_b32_e32 v74, 31, v0
	s_movk_i32 s2, 0x210
	s_lshl_b32 s0, s33, 6
	v_lshlrev_b32_e32 v10, 4, v66
	s_and_b32 s0, s0, 0xffffff80
	v_mad_u32_u24 v75, v74, s2, v10
	v_add_u32_e32 v67, s0, v75
	global_load_dwordx4 v[34:37], v[12:13], off offset:3072
	s_barrier
	ds_read_b128 v[10:13], v67
	ds_read_b128 v[58:61], v67 offset:32
	v_lshlrev_b32_e32 v76, 2, v66
	s_lshl_b32 s0, s33, 5
	s_movk_i32 s3, 0x1000
	s_waitcnt vmcnt(7) lgkmcnt(1)
	v_mfma_f32_32x32x16_f16 v[18:33], v[2:5], v[10:13], 0
	ds_read_b128 v[2:5], v67 offset:256
	ds_read_b128 v[62:65], v67 offset:288
	s_waitcnt vmcnt(6) lgkmcnt(1)
	v_mfma_f32_32x32x16_f16 v[2:17], v[6:9], v[2:5], 0
	s_waitcnt vmcnt(5)
	v_mfma_f32_32x32x16_f16 v[18:33], v[42:45], v[58:61], v[18:33]
	ds_read_b128 v[42:45], v67 offset:64
	s_waitcnt vmcnt(4) lgkmcnt(1)
	v_mfma_f32_32x32x16_f16 v[2:17], v[46:49], v[62:65], v[2:17]
	ds_read_b128 v[62:65], v67 offset:96
	ds_read_b128 v[46:49], v67 offset:320
	s_waitcnt vmcnt(3) lgkmcnt(2)
	v_mfma_f32_32x32x16_f16 v[18:33], v[50:53], v[42:45], v[18:33]
	v_mov_b32_e32 v51, v71
	v_or_b32_e32 v50, s0, v76
	v_lshl_add_u64 v[72:73], v[50:51], 2, s[6:7]
	ds_read_b128 v[42:45], v67 offset:352
	s_waitcnt lgkmcnt(0)
	s_barrier
	s_waitcnt vmcnt(2)
	v_mfma_f32_32x32x16_f16 v[2:17], v[54:57], v[46:49], v[2:17]
	global_load_dwordx4 v[46:49], v[72:73], off
	global_load_dwordx4 v[58:61], v[72:73], off offset:32
	global_load_dwordx4 v[66:69], v[72:73], off offset:64
	s_lshl_b64 s[0:1], s[0:1], 10
	s_add_u32 s0, s8, s0
	s_addc_u32 s1, s9, s1
	s_waitcnt vmcnt(4)
	v_mfma_f32_32x32x16_f16 v[18:33], v[38:41], v[62:65], v[18:33]
	global_load_dwordx4 v[62:65], v[72:73], off offset:96
	v_lshlrev_b32_e32 v38, 1, v50
	v_mad_u32_u24 v77, v74, s2, v38
	global_load_dwordx4 v[50:53], v[72:73], off offset:512
	global_load_dwordx4 v[54:57], v[72:73], off offset:544
	global_load_dwordx4 v[38:41], v[72:73], off offset:576
	s_waitcnt vmcnt(6)
	s_nop 4
	v_pk_add_f32 v[18:19], v[46:47], v[18:19]
	v_mfma_f32_32x32x16_f16 v[2:17], v[34:37], v[42:45], v[2:17]
	s_waitcnt vmcnt(5)
	v_add_f32_e64 v34, v58, v22
	v_add_f32_e64 v35, v59, v23
	v_add_f32_e64 v20, v48, v20
	v_add_f32_e64 v21, v49, v21
	v_mul_f32_e32 v42, 0x3fb8aa3b, v34
	v_mul_f32_e32 v36, 0x3fb8aa3b, v20
	v_mul_f32_e32 v37, 0x3fb8aa3b, v21
	v_exp_f32_e32 v36, v36
	v_exp_f32_e32 v37, v37
	v_mul_f32_e32 v43, 0x3fb8aa3b, v35
	s_waitcnt vmcnt(3)
	v_pk_add_f32 v[22:23], v[62:63], v[30:31]
	v_mul_f32_e32 v30, 0x3fb8aa3b, v18
	v_mul_f32_e32 v31, 0x3fb8aa3b, v19
	v_exp_f32_e32 v30, v30
	v_exp_f32_e32 v31, v31
	v_pk_add_f32 v[24:25], v[60:61], v[24:25]
	v_exp_f32_e32 v42, v42
	v_exp_f32_e32 v43, v43
	v_pk_add_f32 v[30:31], v[30:31], -1.0 op_sel_hi:[1,0]
	v_cmp_lt_f32_e32 vcc, 0, v19
	v_mul_f32_e32 v44, 0x3fb8aa3b, v24
	v_mul_f32_e32 v45, 0x3fb8aa3b, v25
	v_cndmask_b32_e32 v19, v31, v19, vcc
	v_cmp_lt_f32_e32 vcc, 0, v18
	v_pk_add_f32 v[26:27], v[66:67], v[26:27]
	v_exp_f32_e32 v44, v44
	v_exp_f32_e32 v45, v45
	v_pk_add_f32 v[36:37], v[36:37], -1.0 op_sel_hi:[1,0]
	v_cndmask_b32_e32 v18, v30, v18, vcc
	v_cmp_lt_f32_e32 vcc, 0, v21
	v_mul_f32_e32 v46, 0x3fb8aa3b, v26
	v_mul_f32_e32 v47, 0x3fb8aa3b, v27
	v_cndmask_b32_e32 v21, v37, v21, vcc
	v_cmp_lt_f32_e32 vcc, 0, v20
	v_pk_add_f32 v[28:29], v[68:69], v[28:29]
	v_exp_f32_e32 v46, v46
	v_exp_f32_e32 v47, v47
	v_pk_add_f32 v[42:43], v[42:43], -1.0 op_sel_hi:[1,0]
	v_cndmask_b32_e32 v20, v36, v20, vcc
	v_cmp_lt_f32_e32 vcc, 0, v35
	v_mul_f32_e32 v48, 0x3fb8aa3b, v28
	v_mul_f32_e32 v49, 0x3fb8aa3b, v29
	v_cndmask_b32_e32 v30, v43, v35, vcc
	v_cmp_lt_f32_e32 vcc, 0, v34
	v_exp_f32_e32 v48, v48
	v_exp_f32_e32 v49, v49
	v_pk_add_f32 v[44:45], v[44:45], -1.0 op_sel_hi:[1,0]
	v_cndmask_b32_e32 v31, v42, v34, vcc
	v_cmp_lt_f32_e32 vcc, 0, v25
	v_pk_add_f32 v[46:47], v[46:47], -1.0 op_sel_hi:[1,0]
	v_pk_add_f32 v[48:49], v[48:49], -1.0 op_sel_hi:[1,0]
	v_cndmask_b32_e32 v25, v45, v25, vcc
	v_cmp_lt_f32_e32 vcc, 0, v24
	v_cvt_pk_f16_f32 v18, v18, v19
	v_cvt_pk_f16_f32 v19, v20, v21
	v_cndmask_b32_e32 v24, v44, v24, vcc
	v_cmp_lt_f32_e32 vcc, 0, v27
	v_cvt_pk_f16_f32 v20, v31, v30
	v_cvt_pk_f16_f32 v21, v24, v25
	v_cndmask_b32_e32 v27, v47, v27, vcc
	v_cmp_lt_f32_e32 vcc, 0, v26
	ds_write2_b64 v77, v[18:19], v[20:21] offset1:2
	v_mul_f32_e32 v18, 0x3fb8aa3b, v23
	v_cndmask_b32_e32 v26, v46, v26, vcc
	v_cmp_lt_f32_e32 vcc, 0, v29
	v_exp_f32_e32 v59, v18
	v_mul_f32_e32 v58, 0x3fb8aa3b, v22
	v_cndmask_b32_e32 v29, v49, v29, vcc
	v_cmp_lt_f32_e32 vcc, 0, v28
	v_exp_f32_e32 v58, v58
	v_cvt_pk_f16_f32 v24, v26, v27
	v_cndmask_b32_e32 v18, v48, v28, vcc
	v_cvt_pk_f16_f32 v25, v18, v29
	v_pk_add_f32 v[28:29], v[64:65], v[32:33]
	v_pk_add_f32 v[26:27], v[58:59], -1.0 op_sel_hi:[1,0]
	v_mul_f32_e32 v18, 0x3fb8aa3b, v28
	v_exp_f32_e32 v30, v18
	v_mul_f32_e32 v18, 0x3fb8aa3b, v29
	v_exp_f32_e32 v31, v18
	v_cmp_lt_f32_e32 vcc, 0, v23
	global_load_dwordx4 v[18:21], v[72:73], off offset:608
	s_waitcnt vmcnt(3)
	v_pk_add_f32 v[2:3], v[50:51], v[2:3]
	v_cndmask_b32_e32 v23, v27, v23, vcc
	v_cmp_lt_f32_e32 vcc, 0, v22
	v_pk_add_f32 v[4:5], v[52:53], v[4:5]
	s_waitcnt vmcnt(2)
	v_pk_add_f32 v[6:7], v[54:55], v[6:7]
	v_cndmask_b32_e32 v22, v26, v22, vcc
	v_pk_add_f32 v[26:27], v[30:31], -1.0 op_sel_hi:[1,0]
	v_cmp_lt_f32_e32 vcc, 0, v29
	v_cvt_pk_f16_f32 v22, v22, v23
	v_pk_add_f32 v[8:9], v[56:57], v[8:9]
	v_cndmask_b32_e32 v23, v27, v29, vcc
	v_mul_f32_e32 v27, 0x3fb8aa3b, v2
	v_exp_f32_e32 v30, v27
	v_mul_f32_e32 v27, 0x3fb8aa3b, v3
	v_exp_f32_e32 v31, v27
	v_cmp_lt_f32_e32 vcc, 0, v28
	s_waitcnt vmcnt(1)
	v_pk_add_f32 v[10:11], v[38:39], v[10:11]
	v_cndmask_b32_e32 v26, v26, v28, vcc
	v_cvt_pk_f16_f32 v23, v26, v23
	ds_write2_b64 v77, v[24:25], v[22:23] offset0:4 offset1:6
	v_pk_add_f32 v[22:23], v[30:31], -1.0 op_sel_hi:[1,0]
	v_cmp_lt_f32_e32 vcc, 0, v3
	global_load_dwordx4 v[26:29], v70, s[0:1] offset:2048
	s_nop 0
	v_cndmask_b32_e32 v3, v23, v3, vcc
	v_mul_f32_e32 v23, 0x3fb8aa3b, v4
	v_exp_f32_e32 v24, v23
	v_mul_f32_e32 v23, 0x3fb8aa3b, v5
	v_exp_f32_e32 v25, v23
	v_cmp_lt_f32_e32 vcc, 0, v2
	s_nop 1
	v_cndmask_b32_e32 v2, v22, v2, vcc
	v_cvt_pk_f16_f32 v30, v2, v3
	v_pk_add_f32 v[2:3], v[24:25], -1.0 op_sel_hi:[1,0]
	v_cmp_lt_f32_e32 vcc, 0, v5
	s_nop 1
	v_cndmask_b32_e32 v3, v3, v5, vcc
	v_mul_f32_e32 v5, 0x3fb8aa3b, v6
	v_exp_f32_e32 v22, v5
	v_mul_f32_e32 v5, 0x3fb8aa3b, v7
	v_cmp_lt_f32_e32 vcc, 0, v4
	v_exp_f32_e32 v23, v5
	s_nop 0
	v_cndmask_b32_e32 v2, v2, v4, vcc
	v_cvt_pk_f16_f32 v31, v2, v3
	v_mul_f32_e32 v2, 0x3fb8aa3b, v8
	v_exp_f32_e32 v24, v2
	global_load_dwordx4 v[2:5], v70, s[0:1]
	v_pk_add_f32 v[22:23], v[22:23], -1.0 op_sel_hi:[1,0]
	v_cmp_lt_f32_e32 vcc, 0, v7
	s_nop 1
	v_cndmask_b32_e32 v7, v23, v7, vcc
	v_mul_f32_e32 v23, 0x3fb8aa3b, v9
	v_exp_f32_e32 v25, v23
	v_cmp_lt_f32_e32 vcc, 0, v6
	v_pk_add_f32 v[32:33], v[24:25], -1.0 op_sel_hi:[1,0]
	s_nop 0
	v_cndmask_b32_e32 v6, v22, v6, vcc
	global_load_dwordx4 v[22:25], v70, s[0:1] offset:1024
	v_cmp_lt_f32_e32 vcc, 0, v9
	v_cvt_pk_f16_f32 v6, v6, v7
	s_nop 0
	v_cndmask_b32_e32 v7, v33, v9, vcc
	v_mul_f32_e32 v9, 0x3fb8aa3b, v10
	v_exp_f32_e32 v34, v9
	v_mul_f32_e32 v9, 0x3fb8aa3b, v11
	v_exp_f32_e32 v35, v9
	v_cmp_lt_f32_e32 vcc, 0, v8
	s_nop 1
	v_cndmask_b32_e32 v8, v32, v8, vcc
	v_cvt_pk_f16_f32 v7, v8, v7
	ds_write2_b64 v77, v[30:31], v[6:7] offset0:32 offset1:34
	v_pk_add_f32 v[6:7], v[34:35], -1.0 op_sel_hi:[1,0]
	v_cmp_lt_f32_e32 vcc, 0, v11
	v_pk_add_f32 v[8:9], v[40:41], v[12:13]
	v_lshl_add_u64 v[34:35], s[0:1], 0, v[70:71]
	v_cndmask_b32_e32 v7, v7, v11, vcc
	v_mul_f32_e32 v11, 0x3fb8aa3b, v8
	v_exp_f32_e32 v12, v11
	v_mul_f32_e32 v11, 0x3fb8aa3b, v9
	v_exp_f32_e32 v13, v11
	v_cmp_lt_f32_e32 vcc, 0, v10
	s_nop 1
	v_cndmask_b32_e32 v6, v6, v10, vcc
	v_pk_add_f32 v[10:11], v[12:13], -1.0 op_sel_hi:[1,0]
	v_cmp_lt_f32_e32 vcc, 0, v9
	s_waitcnt vmcnt(3)
	v_pk_add_f32 v[12:13], v[18:19], v[14:15]
	v_cvt_pk_f16_f32 v6, v6, v7
	v_cndmask_b32_e32 v7, v11, v9, vcc
	v_mul_f32_e32 v9, 0x3fb8aa3b, v12
	v_exp_f32_e32 v14, v9
	v_mul_f32_e32 v9, 0x3fb8aa3b, v13
	v_exp_f32_e32 v15, v9
	v_cmp_lt_f32_e32 vcc, 0, v8
	s_nop 1
	v_cndmask_b32_e32 v8, v10, v8, vcc
	v_cvt_pk_f16_f32 v7, v8, v7
	v_pk_add_f32 v[8:9], v[14:15], -1.0 op_sel_hi:[1,0]
	v_cmp_lt_f32_e32 vcc, 0, v13
	v_pk_add_f32 v[10:11], v[20:21], v[16:17]
	s_nop 0
	v_cndmask_b32_e32 v9, v9, v13, vcc
	v_mul_f32_e32 v13, 0x3fb8aa3b, v10
	v_exp_f32_e32 v14, v13
	v_mul_f32_e32 v13, 0x3fb8aa3b, v11
	v_exp_f32_e32 v15, v13
	v_cmp_lt_f32_e32 vcc, 0, v12
	s_nop 1
	v_cndmask_b32_e32 v8, v8, v12, vcc
	v_pk_add_f32 v[12:13], v[14:15], -1.0 op_sel_hi:[1,0]
	v_cmp_lt_f32_e32 vcc, 0, v11
	v_cvt_pk_f16_f32 v8, v8, v9
	s_nop 0
	v_cndmask_b32_e32 v9, v13, v11, vcc
	v_cmp_lt_f32_e32 vcc, 0, v10
	s_nop 1
	v_cndmask_b32_e32 v10, v12, v10, vcc
	v_cvt_pk_f16_f32 v9, v10, v9
	ds_write2_b64 v77, v[6:7], v[8:9] offset0:36 offset1:38
	v_add_co_u32_e32 v6, vcc, s3, v34
	s_movk_i32 s3, 0x2000
	s_nop 0
	v_addc_co_u32_e32 v7, vcc, 0, v35, vcc
	v_add_co_u32_e32 v60, vcc, s3, v34
	s_nop 1
	v_addc_co_u32_e32 v61, vcc, 0, v35, vcc
	global_load_dwordx4 v[18:21], v70, s[0:1] offset:3072
	global_load_dwordx4 v[30:33], v[60:61], off offset:-4096
	global_load_dwordx4 v[36:39], v[6:7], off offset:1024
	global_load_dwordx4 v[40:43], v[6:7], off offset:2048
	global_load_dwordx4 v[44:47], v[6:7], off offset:3072
	s_waitcnt lgkmcnt(0)
	s_barrier
	ds_read_b128 v[6:9], v75
	ds_read_b128 v[48:51], v75 offset:32
	s_waitcnt vmcnt(6) lgkmcnt(1)
	v_mfma_f32_32x32x16_f16 v[2:17], v[2:5], v[6:9], 0
	s_waitcnt vmcnt(5) lgkmcnt(0)
	v_mfma_f32_32x32x16_f16 v[2:17], v[22:25], v[48:51], v[2:17]
	ds_read_b128 v[22:25], v75 offset:64
	global_load_dwordx4 v[48:51], v[60:61], off
	global_load_dwordx4 v[52:55], v[60:61], off offset:1024
	ds_read_b128 v[56:59], v75 offset:96
	s_waitcnt lgkmcnt(1)
	v_mfma_f32_32x32x16_f16 v[2:17], v[26:29], v[22:25], v[2:17]
	global_load_dwordx4 v[22:25], v[60:61], off offset:2048
	global_load_dwordx4 v[26:29], v[60:61], off offset:3072
	s_waitcnt vmcnt(8) lgkmcnt(0)
	v_mfma_f32_32x32x16_f16 v[2:17], v[18:21], v[56:59], v[2:17]
	ds_read_b128 v[18:21], v75 offset:128
	ds_read_b128 v[56:59], v75 offset:160
	s_movk_i32 s0, 0x3000
	s_movk_i32 s1, 0x4000
	s_waitcnt vmcnt(7) lgkmcnt(1)
	v_mfma_f32_32x32x16_f16 v[2:17], v[30:33], v[18:21], v[2:17]
	ds_read_b128 v[18:21], v75 offset:192
	ds_read_b128 v[30:33], v75 offset:224
	s_waitcnt vmcnt(6) lgkmcnt(2)
	v_mfma_f32_32x32x16_f16 v[2:17], v[36:39], v[56:59], v[2:17]
	v_add_co_u32_e32 v56, vcc, s0, v34
	s_nop 1
	v_addc_co_u32_e32 v57, vcc, 0, v35, vcc
	v_add_co_u32_e32 v64, vcc, s1, v34
	s_waitcnt vmcnt(5) lgkmcnt(1)
	v_mfma_f32_32x32x16_f16 v[2:17], v[40:43], v[18:21], v[2:17]
	v_addc_co_u32_e32 v65, vcc, 0, v35, vcc
	global_load_dwordx4 v[18:21], v[56:57], off offset:1024
	global_load_dwordx4 v[36:39], v[56:57], off offset:2048
	global_load_dwordx4 v[40:43], v[64:65], off offset:-4096
	s_nop 0
	global_load_dwordx4 v[56:59], v[56:57], off offset:3072
	s_waitcnt vmcnt(8) lgkmcnt(0)
	v_mfma_f32_32x32x16_f16 v[2:17], v[44:47], v[30:33], v[2:17]
	ds_read_b128 v[30:33], v75 offset:256
	ds_read_b128 v[44:47], v75 offset:288
	s_waitcnt vmcnt(7) lgkmcnt(1)
	v_mfma_f32_32x32x16_f16 v[2:17], v[48:51], v[30:33], v[2:17]
	ds_read_b128 v[30:33], v75 offset:320
	s_waitcnt vmcnt(6) lgkmcnt(1)
	v_mfma_f32_32x32x16_f16 v[2:17], v[52:55], v[44:47], v[2:17]
	global_load_dwordx4 v[44:47], v[64:65], off
	global_load_dwordx4 v[48:51], v[64:65], off offset:1024
	ds_read_b128 v[52:55], v75 offset:352
	global_load_dwordx4 v[60:63], v[64:65], off offset:2048
	s_nop 0
	global_load_dwordx4 v[64:67], v[64:65], off offset:3072
	s_waitcnt vmcnt(9) lgkmcnt(1)
	v_mfma_f32_32x32x16_f16 v[2:17], v[22:25], v[30:33], v[2:17]
	s_waitcnt vmcnt(8) lgkmcnt(0)
	v_mfma_f32_32x32x16_f16 v[2:17], v[26:29], v[52:55], v[2:17]
	ds_read_b128 v[22:25], v75 offset:384
	ds_read_b128 v[26:29], v75 offset:416
	s_movk_i32 s0, 0x5000
	s_movk_i32 s1, 0x6000
	s_waitcnt vmcnt(5) lgkmcnt(1)
	v_mfma_f32_32x32x16_f16 v[2:17], v[40:43], v[22:25], v[2:17]
	s_waitcnt lgkmcnt(0)
	v_mfma_f32_32x32x16_f16 v[2:17], v[18:21], v[26:29], v[2:17]
	ds_read_b128 v[18:21], v75 offset:448
	ds_read_b128 v[22:25], v75 offset:480
	v_add_co_u32_e32 v26, vcc, s0, v34
	s_nop 1
	v_addc_co_u32_e32 v27, vcc, 0, v35, vcc
	v_add_co_u32_e32 v68, vcc, s1, v34
	s_waitcnt lgkmcnt(1)
	v_mfma_f32_32x32x16_f16 v[2:17], v[36:39], v[18:21], v[2:17]
	v_addc_co_u32_e32 v69, vcc, 0, v35, vcc
	global_load_dwordx4 v[36:39], v[26:27], off offset:1024
	global_load_dwordx4 v[40:43], v[26:27], off offset:2048
	global_load_dwordx4 v[52:55], v[68:69], off offset:-4096
	global_load_dwordx4 v[78:81], v[26:27], off offset:3072
	s_waitcnt vmcnt(8) lgkmcnt(0)
	v_mfma_f32_32x32x16_f16 v[2:17], v[56:59], v[22:25], v[2:17]
	ds_read_b128 v[18:21], v75
	ds_read_b128 v[56:59], v75 offset:32
	s_waitcnt vmcnt(7) lgkmcnt(1)
	v_mfma_f32_32x32x16_f16 v[18:33], v[44:47], v[18:21], 0
	ds_read_b128 v[44:47], v75 offset:64
	s_waitcnt vmcnt(6) lgkmcnt(1)
	v_mfma_f32_32x32x16_f16 v[18:33], v[48:51], v[56:59], v[18:33]
	global_load_dwordx4 v[48:51], v[68:69], off
	global_load_dwordx4 v[56:59], v[68:69], off offset:1024
	ds_read_b128 v[82:85], v75 offset:96
	s_waitcnt vmcnt(7) lgkmcnt(1)
	v_mfma_f32_32x32x16_f16 v[18:33], v[60:63], v[44:47], v[18:33]
	global_load_dwordx4 v[44:47], v[68:69], off offset:2048
	global_load_dwordx4 v[60:63], v[68:69], off offset:3072
	s_waitcnt vmcnt(8) lgkmcnt(0)
	v_mfma_f32_32x32x16_f16 v[18:33], v[64:67], v[82:85], v[18:33]
	ds_read_b128 v[64:67], v75 offset:128
	ds_read_b128 v[82:85], v75 offset:160
	s_movk_i32 s0, 0x7000
	v_add_co_u32_e32 v68, vcc, s0, v34
	s_waitcnt vmcnt(5) lgkmcnt(1)
	v_mfma_f32_32x32x16_f16 v[18:33], v[52:55], v[64:67], v[18:33]
	v_addc_co_u32_e32 v69, vcc, 0, v35, vcc
	s_waitcnt lgkmcnt(0)
	v_mfma_f32_32x32x16_f16 v[18:33], v[36:39], v[82:85], v[18:33]
	ds_read_b128 v[36:39], v75 offset:192
	ds_read_b128 v[52:55], v75 offset:224
	global_load_dwordx4 v[64:67], v[68:69], off
	global_load_dwordx4 v[82:85], v[68:69], off offset:1024
	s_waitcnt lgkmcnt(1)
	v_mfma_f32_32x32x16_f16 v[18:33], v[40:43], v[36:39], v[18:33]
	global_load_dwordx4 v[34:37], v[68:69], off offset:2048
	global_load_dwordx4 v[38:41], v[68:69], off offset:3072
	s_waitcnt vmcnt(8) lgkmcnt(0)
	v_mfma_f32_32x32x16_f16 v[18:33], v[78:81], v[52:55], v[18:33]
	ds_read_b128 v[52:55], v75 offset:256
	ds_read_b128 v[78:81], v75 offset:288
	s_waitcnt vmcnt(7) lgkmcnt(1)
	v_mfma_f32_32x32x16_f16 v[18:33], v[48:51], v[52:55], v[18:33]
	ds_read_b128 v[48:51], v75 offset:320
	ds_read_b128 v[52:55], v75 offset:352
	s_waitcnt vmcnt(6) lgkmcnt(2)
	v_mfma_f32_32x32x16_f16 v[18:33], v[56:59], v[78:81], v[18:33]
	s_waitcnt vmcnt(5) lgkmcnt(1)
	v_mfma_f32_32x32x16_f16 v[18:33], v[44:47], v[48:51], v[18:33]
	s_waitcnt vmcnt(4) lgkmcnt(0)
	v_mfma_f32_32x32x16_f16 v[18:33], v[60:63], v[52:55], v[18:33]
	ds_read_b128 v[42:45], v75 offset:384
	ds_read_b128 v[46:49], v75 offset:416
	s_waitcnt vmcnt(3) lgkmcnt(1)
	v_mfma_f32_32x32x16_f16 v[18:33], v[64:67], v[42:45], v[18:33]
	s_waitcnt vmcnt(2) lgkmcnt(0)
	v_mfma_f32_32x32x16_f16 v[18:33], v[82:85], v[46:49], v[18:33]
	ds_read_b128 v[42:45], v75 offset:448
	ds_read_b128 v[46:49], v75 offset:480
	s_waitcnt vmcnt(1) lgkmcnt(1)
	v_mfma_f32_32x32x16_f16 v[18:33], v[34:37], v[42:45], v[18:33]
	s_waitcnt vmcnt(0) lgkmcnt(0)
	v_mfma_f32_32x32x16_f16 v[18:33], v[38:41], v[46:49], v[18:33]
	s_and_b32 s0, s49, 0xffffffc0
	v_or_b32_e32 v35, s0, v76
	v_lshlrev_b32_e32 v34, 2, v35
	s_barrier
	ds_read_b128 v[36:39], v34 offset:25600
	ds_read_b128 v[40:43], v34 offset:25632
	ds_read_b128 v[44:47], v34 offset:26624
	v_cmp_lt_u32_e32 vcc, 31, v1
	s_waitcnt lgkmcnt(2)
	v_mul_f32_e32 v37, v3, v37
	v_fmac_f32_e32 v37, v2, v36
	v_fmac_f32_e32 v37, v4, v38
	v_fmac_f32_e32 v37, v5, v39
	v_add_f32_e32 v48, 0, v37
	ds_read_b128 v[36:39], v34 offset:26656
	s_waitcnt lgkmcnt(1)
	v_mul_f32_e32 v45, v3, v45
	v_fmac_f32_e32 v45, v2, v44
	v_fmac_f32_e32 v45, v4, v46
	v_fmac_f32_e32 v45, v5, v47
	v_cvt_pk_f16_f32 v5, v4, v5
	v_cvt_pk_f16_f32 v4, v2, v3
	v_lshlrev_b32_e32 v2, 1, v35
	v_mul_f32_e32 v3, v7, v41
	s_waitcnt lgkmcnt(0)
	v_mul_f32_e32 v35, v7, v37
	v_fmac_f32_e32 v3, v6, v40
	v_fmac_f32_e32 v35, v6, v36
	v_fmac_f32_e32 v3, v8, v42
	v_fmac_f32_e32 v35, v8, v38
	v_mad_u32_u24 v2, v74, s2, v2
	v_fmac_f32_e32 v3, v9, v43
	v_fmac_f32_e32 v35, v9, v39
	v_cvt_pk_f16_f32 v9, v8, v9
	v_cvt_pk_f16_f32 v8, v6, v7
	ds_read_b128 v[36:39], v34 offset:25664
	ds_write2_b64 v2, v[4:5], v[8:9] offset1:2
	ds_read_b128 v[4:7], v34 offset:26688
	ds_read_b128 v[40:43], v34 offset:25696
	v_add_f32_e32 v44, 0, v45
	v_add_f32_e32 v35, v44, v35
	s_waitcnt lgkmcnt(3)
	v_mul_f32_e32 v8, v11, v37
	s_waitcnt lgkmcnt(1)
	v_mul_f32_e32 v5, v11, v5
	v_fmac_f32_e32 v8, v10, v36
	v_fmac_f32_e32 v5, v10, v4
	v_fmac_f32_e32 v8, v12, v38
	v_fmac_f32_e32 v5, v12, v6
	v_fmac_f32_e32 v8, v13, v39
	ds_read_b128 v[36:39], v34 offset:26720
	v_fmac_f32_e32 v5, v13, v7
	v_add_f32_e32 v4, v35, v5
	s_waitcnt lgkmcnt(1)
	v_mul_f32_e32 v5, v15, v41
	v_fmac_f32_e32 v5, v14, v40
	v_add_f32_e32 v3, v48, v3
	v_fmac_f32_e32 v5, v16, v42
	v_add_f32_e32 v3, v3, v8
	v_fmac_f32_e32 v5, v17, v43
	v_add_f32_e32 v3, v3, v5
	s_waitcnt lgkmcnt(0)
	v_mul_f32_e32 v5, v15, v37
	v_fmac_f32_e32 v5, v14, v36
	v_fmac_f32_e32 v5, v16, v38
	v_fmac_f32_e32 v5, v17, v39
	v_add_f32_e32 v35, v4, v5
	ds_read_b128 v[4:7], v34 offset:25728
	v_cvt_pk_f16_f32 v9, v12, v13
	v_cvt_pk_f16_f32 v8, v10, v11
	v_cvt_pk_f16_f32 v11, v16, v17
	v_cvt_pk_f16_f32 v10, v14, v15
	s_waitcnt lgkmcnt(0)
	v_mul_f32_e32 v5, v19, v5
	v_fmac_f32_e32 v5, v18, v4
	v_fmac_f32_e32 v5, v20, v6
	ds_write2_b64 v2, v[8:9], v[10:11] offset0:4 offset1:6
	v_fmac_f32_e32 v5, v21, v7
	ds_read_b128 v[8:11], v34 offset:26752
	ds_read_b128 v[12:15], v34 offset:25760
	v_add_f32_e32 v3, v3, v5
	ds_read_b128 v[4:7], v34 offset:26784
	s_waitcnt lgkmcnt(2)
	v_mul_f32_e32 v9, v19, v9
	v_fmac_f32_e32 v9, v18, v8
	v_fmac_f32_e32 v9, v20, v10
	s_waitcnt lgkmcnt(0)
	v_mul_f32_e32 v5, v23, v5
	v_fmac_f32_e32 v5, v22, v4
	v_fmac_f32_e32 v9, v21, v11
	v_fmac_f32_e32 v5, v24, v6
	v_add_f32_e32 v10, v35, v9
	v_fmac_f32_e32 v5, v25, v7
	v_add_f32_e32 v16, v10, v5
	ds_read_b128 v[4:7], v34 offset:25792
	v_mul_f32_e32 v11, v23, v13
	v_fmac_f32_e32 v11, v22, v12
	v_fmac_f32_e32 v11, v24, v14
	v_fmac_f32_e32 v11, v25, v15
	s_waitcnt lgkmcnt(0)
	v_mul_f32_e32 v5, v27, v5
	v_cvt_pk_f16_f32 v9, v20, v21
	v_cvt_pk_f16_f32 v8, v18, v19
	v_add_f32_e32 v3, v3, v11
	v_cvt_pk_f16_f32 v11, v24, v25
	v_cvt_pk_f16_f32 v10, v22, v23
	v_fmac_f32_e32 v5, v26, v4
	ds_write2_b64 v2, v[8:9], v[10:11] offset0:8 offset1:10
	v_fmac_f32_e32 v5, v28, v6
	ds_read_b128 v[8:11], v34 offset:25824
	ds_read_b128 v[12:15], v34 offset:26816
	v_fmac_f32_e32 v5, v29, v7
	v_add_f32_e32 v3, v3, v5
	ds_read_b128 v[4:7], v34 offset:26848
	s_waitcnt lgkmcnt(2)
	v_mul_f32_e32 v9, v31, v9
	s_waitcnt lgkmcnt(1)
	v_mul_f32_e32 v13, v27, v13
	v_fmac_f32_e32 v13, v26, v12
	v_fmac_f32_e32 v13, v28, v14
	s_waitcnt lgkmcnt(0)
	v_mul_f32_e32 v5, v31, v5
	v_fmac_f32_e32 v5, v30, v4
	v_fmac_f32_e32 v13, v29, v15
	v_fmac_f32_e32 v9, v30, v8
	v_fmac_f32_e32 v5, v32, v6
	v_add_f32_e32 v14, v16, v13
	v_fmac_f32_e32 v9, v32, v10
	v_fmac_f32_e32 v5, v33, v7
	v_cvt_pk_f16_f32 v13, v28, v29
	v_cvt_pk_f16_f32 v12, v26, v27
	v_fmac_f32_e32 v9, v33, v11
	v_add_f32_e32 v6, v14, v5
	v_cvt_pk_f16_f32 v5, v32, v33
	v_cvt_pk_f16_f32 v4, v30, v31
	v_add_f32_e32 v3, v3, v9
	ds_write2_b64 v2, v[12:13], v[4:5] offset0:12 offset1:14
	v_or_b32_e32 v4, s48, v74
	s_nop 1
	v_permlane32_swap_b32 v3, v6
	v_lshl_add_u32 v70, v4, 2, s33
	v_add_f32_e32 v2, v3, v6
	s_and_saveexec_b64 s[2:3], vcc
	s_xor_b64 s[2:3], exec, s[2:3]
	s_cbranch_execz .LBB5_70
	v_lshl_add_u64 v[4:5], v[70:71], 2, s[14:15]
	global_store_dword v[4:5], v2, off

amdhsa.kernels:
  - .agpr_count:     0
    .args:
      - .actual_access:  read_only
        .address_space:  global
        .offset:         0
        .size:           8
        .value_kind:     global_buffer
      - .actual_access:  write_only
        .address_space:  global
        .offset:         8
        .size:           8
        .value_kind:     global_buffer
      - .actual_access:  read_only
        .address_space:  global
        .offset:         16
        .size:           8
        .value_kind:     global_buffer
      - .actual_access:  read_only
        .address_space:  global
        .offset:         24
        .size:           8
        .value_kind:     global_buffer
      - .actual_access:  read_only
        .address_space:  global
        .offset:         32
        .size:           8
        .value_kind:     global_buffer
      - .actual_access:  read_only
        .address_space:  global
        .offset:         40
        .size:           8
        .value_kind:     global_buffer
      - .actual_access:  read_only
        .address_space:  global
        .offset:         48
        .size:           8
        .value_kind:     global_buffer
      - .actual_access:  read_only
        .address_space:  global
        .offset:         56
        .size:           8
        .value_kind:     global_buffer
      - .actual_access:  read_only
        .address_space:  global
        .offset:         64
        .size:           8
        .value_kind:     global_buffer
      - .actual_access:  read_only
        .address_space:  global
        .offset:         72
        .size:           8
        .value_kind:     global_buffer
      - .actual_access:  read_only
        .address_space:  global
        .offset:         80
        .size:           8
        .value_kind:     global_buffer
      - .actual_access:  write_only
        .address_space:  global
        .offset:         88
        .size:           8
        .value_kind:     global_buffer
      - .actual_access:  write_only
        .address_space:  global
        .offset:         96
        .size:           8
        .value_kind:     global_buffer
      - .actual_access:  write_only
        .address_space:  global
        .offset:         104
        .size:           8
        .value_kind:     global_buffer
      - .actual_access:  write_only
        .address_space:  global
        .offset:         112
        .size:           8
        .value_kind:     global_buffer
      - .actual_access:  write_only
        .address_space:  global
        .offset:         120
        .size:           8
        .value_kind:     global_buffer
    .group_segment_fixed_size: 1564
    .kernarg_segment_align: 8
    .kernarg_segment_size: 128
    .language:       OpenCL C
    .language_version:
      - 2
      - 0
    .max_flat_workgroup_size: 1024
    .name:           _Z6k_pre1PKiPiPKfS3_S3_S3_S3_S3_S3_S3_S3_PDF16_S4_S4_PfS5_
    .private_segment_fixed_size: 0
    .sgpr_count:     26
    .sgpr_spill_count: 0
    .symbol:         _Z6k_pre1PKiPiPKfS3_S3_S3_S3_S3_S3_S3_S3_PDF16_S4_S4_PfS5_.kd
    .uniform_work_group_size: 1
    .uses_dynamic_stack: false
    .vgpr_count:     64
    .vgpr_spill_count: 0
    .wavefront_size: 64
  - .agpr_count:     0
    .args:
      - .actual_access:  read_only
        .address_space:  global
        .offset:         0
        .size:           8
        .value_kind:     global_buffer
      - .actual_access:  read_only
        .address_space:  global
        .offset:         8
        .size:           8
        .value_kind:     global_buffer
      - .actual_access:  read_only
        .address_space:  global
        .offset:         16
        .size:           8
        .value_kind:     global_buffer
      - .actual_access:  read_only
        .address_space:  global
        .offset:         24
        .size:           8
        .value_kind:     global_buffer
      - .actual_access:  write_only
        .address_space:  global
        .offset:         32
        .size:           8
        .value_kind:     global_buffer
      - .actual_access:  write_only
        .address_space:  global
        .offset:         40
        .size:           8
        .value_kind:     global_buffer
    .group_segment_fixed_size: 1632
    .kernarg_segment_align: 8
    .kernarg_segment_size: 48
    .language:       OpenCL C
    .language_version:
      - 2
      - 0
    .max_flat_workgroup_size: 1024
    .name:           _Z9k_scatterPKiS0_S0_S0_PiS1_
    .private_segment_fixed_size: 0
    .sgpr_count:     22
    .sgpr_spill_count: 0
    .symbol:         _Z9k_scatterPKiS0_S0_S0_PiS1_.kd
    .uniform_work_group_size: 1
    .uses_dynamic_stack: false
    .vgpr_count:     50
    .vgpr_spill_count: 0
    .wavefront_size: 64
  - .agpr_count:     0
    .args:
      - .actual_access:  read_only
        .address_space:  global
        .offset:         0
        .size:           8
        .value_kind:     global_buffer
      - .actual_access:  read_only
        .address_space:  global
        .offset:         8
        .size:           8
        .value_kind:     global_buffer
      - .actual_access:  write_only
        .address_space:  global
        .offset:         16
        .size:           8
        .value_kind:     global_buffer
      - .actual_access:  write_only
        .address_space:  global
        .offset:         24
        .size:           8
        .value_kind:     global_buffer
      - .actual_access:  read_only
        .address_space:  global
        .offset:         32
        .size:           8
        .value_kind:     global_buffer
      - .actual_access:  read_only
        .address_space:  global
        .offset:         40
        .size:           8
        .value_kind:     global_buffer
      - .actual_access:  read_only
        .address_space:  global
        .offset:         48
        .size:           8
        .value_kind:     global_buffer
      - .actual_access:  read_only
        .address_space:  global
        .offset:         56
        .size:           8
        .value_kind:     global_buffer
      - .actual_access:  write_only
        .address_space:  global
        .offset:         64
        .size:           8
        .value_kind:     global_buffer
      - .actual_access:  write_only
        .address_space:  global
        .offset:         72
        .size:           8
        .value_kind:     global_buffer
      - .actual_access:  write_only
        .address_space:  global
        .offset:         80
        .size:           8
        .value_kind:     global_buffer
    .group_segment_fixed_size: 38720
    .kernarg_segment_align: 8
    .kernarg_segment_size: 88
    .language:       OpenCL C
    .language_version:
      - 2
      - 0
    .max_flat_workgroup_size: 1024
    .name:           _Z5k_csrPKiS0_PiS1_PKfS3_S3_S3_PDF16_P15HIP_vector_typeIfLj4EES7_
    .private_segment_fixed_size: 0
    .sgpr_count:     86
    .sgpr_spill_count: 0
    .symbol:         _Z5k_csrPKiS0_PiS1_PKfS3_S3_S3_PDF16_P15HIP_vector_typeIfLj4EES7_.kd
    .uniform_work_group_size: 1
    .uses_dynamic_stack: false
    .vgpr_count:     64
    .vgpr_spill_count: 0
    .wavefront_size: 64
  - .agpr_count:     0
    .args:
      - .actual_access:  read_only
        .address_space:  global
        .offset:         0
        .size:           8
        .value_kind:     global_buffer
      - .actual_access:  write_only
        .address_space:  global
        .offset:         8
        .size:           8
        .value_kind:     global_buffer
      - .actual_access:  write_only
        .address_space:  global
        .offset:         16
        .size:           8
        .value_kind:     global_buffer
    .group_segment_fixed_size: 16
    .kernarg_segment_align: 8
    .kernarg_segment_size: 24
    .language:       OpenCL C
    .language_version:
      - 2
      - 0
    .max_flat_workgroup_size: 256
    .name:           _Z6k_pre2PKiPiS1_
    .private_segment_fixed_size: 0
    .sgpr_count:     14
    .sgpr_spill_count: 0
    .symbol:         _Z6k_pre2PKiPiS1_.kd
    .uniform_work_group_size: 1
    .uses_dynamic_stack: false
    .vgpr_count:     14
    .vgpr_spill_count: 0
    .wavefront_size: 64
  - .agpr_count:     0
    .args:
      - .actual_access:  read_only
        .address_space:  global
        .offset:         0
        .size:           8
        .value_kind:     global_buffer
      - .actual_access:  read_only
        .address_space:  global
        .offset:         8
        .size:           8
        .value_kind:     global_buffer
      - .actual_access:  read_only
        .address_space:  global
        .offset:         16
        .size:           8
        .value_kind:     global_buffer
      - .actual_access:  read_only
        .address_space:  global
        .offset:         24
        .size:           8
        .value_kind:     global_buffer
      - .actual_access:  read_only
        .address_space:  global
        .offset:         32
        .size:           8
        .value_kind:     global_buffer
      - .actual_access:  write_only
        .address_space:  global
        .offset:         40
        .size:           8
        .value_kind:     global_buffer
    .group_segment_fixed_size: 1408
    .kernarg_segment_align: 8
    .kernarg_segment_size: 48
    .language:       OpenCL C
    .language_version:
      - 2
      - 0
    .max_flat_workgroup_size: 256
    .name:           _Z7k_finalPKfS0_S0_S0_S0_Pf
    .private_segment_fixed_size: 0
    .sgpr_count:     14
    .sgpr_spill_count: 0
    .symbol:         _Z7k_finalPKfS0_S0_S0_S0_Pf.kd
    .uniform_work_group_size: 1
    .uses_dynamic_stack: false
    .vgpr_count:     29
    .vgpr_spill_count: 0
    .wavefront_size: 64
  - .agpr_count:     0
    .args:
      - .actual_access:  read_only
        .address_space:  global
        .offset:         0
        .size:           8
        .value_kind:     global_buffer
      - .actual_access:  read_only
        .address_space:  global
        .offset:         8
        .size:           8
        .value_kind:     global_buffer
      - .actual_access:  read_only
        .address_space:  global
        .offset:         16
        .size:           8
        .value_kind:     global_buffer
      - .actual_access:  read_only
        .address_space:  global
        .offset:         24
        .size:           8
        .value_kind:     global_buffer
      - .actual_access:  read_only
        .address_space:  global
        .offset:         32
        .size:           8
        .value_kind:     global_buffer
      - .actual_access:  read_only
        .address_space:  global
        .offset:         40
        .size:           8
        .value_kind:     global_buffer
      - .actual_access:  read_only
        .address_space:  global
        .offset:         48
        .size:           8
        .value_kind:     global_buffer
      - .actual_access:  read_only
        .address_space:  global
        .offset:         56
        .size:           8
        .value_kind:     global_buffer
      - .actual_access:  write_only
        .address_space:  global
        .offset:         64
        .size:           8
        .value_kind:     global_buffer
      - .actual_access:  write_only
        .address_space:  global
        .offset:         72
        .size:           8
        .value_kind:     global_buffer
      - .actual_access:  write_only
        .address_space:  global
        .offset:         80
        .size:           8
        .value_kind:     global_buffer
      - .actual_access:  read_only
        .address_space:  global
        .offset:         88
        .size:           8
        .value_kind:     global_buffer
      - .actual_access:  read_only
        .address_space:  global
        .offset:         96
        .size:           8
        .value_kind:     global_buffer
      - .actual_access:  read_only
        .address_space:  global
        .offset:         104
        .size:           8
        .value_kind:     global_buffer
      - .actual_access:  read_only
        .address_space:  global
        .offset:         112
        .size:           8
        .value_kind:     global_buffer
      - .actual_access:  read_only
        .address_space:  global
        .offset:         120
        .size:           8
        .value_kind:     global_buffer
      - .actual_access:  read_only
        .address_space:  global
        .offset:         128
        .size:           8
        .value_kind:     global_buffer
      - .actual_access:  read_only
        .address_space:  global
        .offset:         136
        .size:           8
        .value_kind:     global_buffer
      - .actual_access:  read_only
        .address_space:  global
        .offset:         144
        .size:           8
        .value_kind:     global_buffer
    .group_segment_fixed_size: 29248
    .kernarg_segment_align: 8
    .kernarg_segment_size: 152
    .language:       OpenCL C
    .language_version:
      - 2
      - 0
    .max_flat_workgroup_size: 256
    .name:           _Z7k_layerILi0EEvPKiS1_PKfS3_PKDF16_S3_S5_S5_PDF16_P15HIP_vector_typeIfLj4EES9_S3_S3_S3_S3_S3_S3_PfSA_
    .private_segment_fixed_size: 0
    .sgpr_count:     66
    .sgpr_spill_count: 0
    .symbol:         _Z7k_layerILi0EEvPKiS1_PKfS3_PKDF16_S3_S5_S5_PDF16_P15HIP_vector_typeIfLj4EES9_S3_S3_S3_S3_S3_S3_PfSA_.kd
    .uniform_work_group_size: 1
    .uses_dynamic_stack: false
    .vgpr_count:     86
    .vgpr_spill_count: 0
    .wavefront_size: 64
  - .agpr_count:     0
    .args:
      - .actual_access:  read_only
        .address_space:  global
        .offset:         0
        .size:           8
        .value_kind:     global_buffer
      - .actual_access:  read_only
        .address_space:  global
        .offset:         8
        .size:           8
        .value_kind:     global_buffer
      - .actual_access:  read_only
        .address_space:  global
        .offset:         16
        .size:           8
        .value_kind:     global_buffer
      - .actual_access:  read_only
        .address_space:  global
        .offset:         24
        .size:           8
        .value_kind:     global_buffer
      - .actual_access:  read_only
        .address_space:  global
        .offset:         32
        .size:           8
        .value_kind:     global_buffer
      - .actual_access:  read_only
        .address_space:  global
        .offset:         40
        .size:           8
        .value_kind:     global_buffer
      - .actual_access:  read_only
        .address_space:  global
        .offset:         48
        .size:           8
        .value_kind:     global_buffer
      - .actual_access:  read_only
        .address_space:  global
        .offset:         56
        .size:           8
        .value_kind:     global_buffer
      - .actual_access:  write_only
        .address_space:  global
        .offset:         64
        .size:           8
        .value_kind:     global_buffer
      - .actual_access:  write_only
        .address_space:  global
        .offset:         72
        .size:           8
        .value_kind:     global_buffer
      - .actual_access:  write_only
        .address_space:  global
        .offset:         80
        .size:           8
        .value_kind:     global_buffer
      - .actual_access:  read_only
        .address_space:  global
        .offset:         88
        .size:           8
        .value_kind:     global_buffer
      - .actual_access:  read_only
        .address_space:  global
        .offset:         96
        .size:           8
        .value_kind:     global_buffer
      - .actual_access:  read_only
        .address_space:  global
        .offset:         104
        .size:           8
        .value_kind:     global_buffer
      - .actual_access:  read_only
        .address_space:  global
        .offset:         112
        .size:           8
        .value_kind:     global_buffer
      - .actual_access:  read_only
        .address_space:  global
        .offset:         120
        .size:           8
        .value_kind:     global_buffer
      - .actual_access:  read_only
        .address_space:  global
        .offset:         128
        .size:           8
        .value_kind:     global_buffer
      - .actual_access:  read_only
        .address_space:  global
        .offset:         136
        .size:           8
        .value_kind:     global_buffer
      - .actual_access:  read_only
        .address_space:  global
        .offset:         144
        .size:           8
        .value_kind:     global_buffer
    .group_segment_fixed_size: 21504
    .kernarg_segment_align: 8
    .kernarg_segment_size: 152
    .language:       OpenCL C
    .language_version:
      - 2
      - 0
    .max_flat_workgroup_size: 256
    .name:           _Z7k_layerILi1EEvPKiS1_PKfS3_PKDF16_S3_S5_S5_PDF16_P15HIP_vector_typeIfLj4EES9_S3_S3_S3_S3_S3_S3_PfSA_
    .private_segment_fixed_size: 0
    .sgpr_count:     70
    .sgpr_spill_count: 0
    .symbol:         _Z7k_layerILi1EEvPKiS1_PKfS3_PKDF16_S3_S5_S5_PDF16_P15HIP_vector_typeIfLj4EES9_S3_S3_S3_S3_S3_S3_PfSA_.kd
    .uniform_work_group_size: 1
    .uses_dynamic_stack: false
    .vgpr_count:     96
    .vgpr_spill_count: 0
    .wavefront_size: 64
  - .agpr_count:     0
    .args:
      - .actual_access:  read_only
        .address_space:  global
        .offset:         0
        .size:           8
        .value_kind:     global_buffer
      - .actual_access:  read_only
        .address_space:  global
        .offset:         8
        .size:           8
        .value_kind:     global_buffer
      - .actual_access:  read_only
        .address_space:  global
        .offset:         16
        .size:           8
        .value_kind:     global_buffer
      - .actual_access:  read_only
        .address_space:  global
        .offset:         24
        .size:           8
        .value_kind:     global_buffer
      - .actual_access:  read_only
        .address_space:  global
        .offset:         32
        .size:           8
        .value_kind:     global_buffer
      - .actual_access:  read_only
        .address_space:  global
        .offset:         40
        .size:           8
        .value_kind:     global_buffer
      - .actual_access:  read_only
        .address_space:  global
        .offset:         48
        .size:           8
        .value_kind:     global_buffer
      - .actual_access:  read_only
        .address_space:  global
        .offset:         56
        .size:           8
        .value_kind:     global_buffer
      - .actual_access:  read_only
        .address_space:  global
        .offset:         64
        .size:           8
        .value_kind:     global_buffer
      - .actual_access:  read_only
        .address_space:  global
        .offset:         72
        .size:           8
        .value_kind:     global_buffer
      - .actual_access:  read_only
        .address_space:  global
        .offset:         80
        .size:           8
        .value_kind:     global_buffer
      - .actual_access:  read_only
        .address_space:  global
        .offset:         88
        .size:           8
        .value_kind:     global_buffer
      - .actual_access:  read_only
        .address_space:  global
        .offset:         96
        .size:           8
        .value_kind:     global_buffer
      - .actual_access:  read_only
        .address_space:  global
        .offset:         104
        .size:           8
        .value_kind:     global_buffer
      - .actual_access:  read_only
        .address_space:  global
        .offset:         112
        .size:           8
        .value_kind:     global_buffer
      - .actual_access:  read_only
        .address_space:  global
        .offset:         120
        .size:           8
        .value_kind:     global_buffer
      - .actual_access:  read_only
        .address_space:  global
        .offset:         128
        .size:           8
        .value_kind:     global_buffer
      - .actual_access:  write_only
        .address_space:  global
        .offset:         136
        .size:           8
        .value_kind:     global_buffer
      - .address_space:  global
        .offset:         144
        .size:           8
        .value_kind:     global_buffer
    .group_segment_fixed_size: 19456
    .kernarg_segment_align: 8
    .kernarg_segment_size: 152
    .language:       OpenCL C
    .language_version:
      - 2
      - 0
    .max_flat_workgroup_size: 256
    .name:           _Z7k_layerILi2EEvPKiS1_PKfS3_PKDF16_S3_S5_S5_PDF16_P15HIP_vector_typeIfLj4EES9_S3_S3_S3_S3_S3_S3_PfSA_
    .private_segment_fixed_size: 0
    .sgpr_count:     74
    .sgpr_spill_count: 0
    .symbol:         _Z7k_layerILi2EEvPKiS1_PKfS3_PKDF16_S3_S5_S5_PDF16_P15HIP_vector_typeIfLj4EES9_S3_S3_S3_S3_S3_S3_PfSA_.kd
    .uniform_work_group_size: 1
    .uses_dynamic_stack: false
    .vgpr_count:     110
    .vgpr_spill_count: 0
    .wavefront_size: 64
